# background expert-weight conversion in the NSA tile loop (lean version), placement kept
# baseline (speedup 1.0000x reference)
.LBB0_2419:
	s_lshl_b32 s2, s2, 13
	s_add_i32 s76, s2, 0
	s_add_i32 s76, s76, 0x10000
	s_andn2_b64 vcc, exec, s[8:9]
	v_lshlrev_b32_e32 v134, 2, v162
	s_cbranch_vccnz .LBB0_2468
	v_or_b32_e32 v6, 32, v168
	v_cmp_gt_i32_e64 s[40:41], v6, v2
	v_cmp_lt_i32_e64 s[42:43], v6, v2
	v_or_b32_e32 v6, 34, v168
	v_cmp_gt_i32_e64 s[44:45], v6, v2
	v_or_b32_e32 v6, 35, v168
	v_cmp_gt_i32_e64 s[46:47], v6, v2
	v_or_b32_e32 v6, 40, v168
	v_cmp_gt_i32_e64 s[48:49], v6, v2
	v_or_b32_e32 v6, 41, v168
	v_cmp_gt_i32_e64 s[50:51], v6, v2
	v_or_b32_e32 v6, 42, v168
	v_cmp_gt_i32_e64 s[52:53], v6, v2
	v_or_b32_e32 v6, 43, v168
	v_cmp_gt_i32_e64 s[54:55], v6, v2
	v_or_b32_e32 v6, 48, v168
	v_cmp_gt_i32_e64 s[56:57], v6, v2
	v_or_b32_e32 v6, 49, v168
	v_cmp_gt_i32_e64 s[58:59], v6, v2
	v_or_b32_e32 v6, 50, v168
	v_cmp_gt_i32_e64 s[60:61], v6, v2
	v_or_b32_e32 v6, 51, v168
	v_cmp_gt_i32_e64 s[62:63], v6, v2
	v_or_b32_e32 v6, 56, v168
	v_cmp_gt_i32_e64 s[64:65], v6, v2
	v_or_b32_e32 v6, 57, v168
	v_cmp_gt_i32_e64 s[66:67], v6, v2
	v_or_b32_e32 v6, 58, v168
	v_cmp_gt_i32_e64 s[68:69], v6, v2
	v_or_b32_e32 v6, 59, v168
	v_cmp_gt_i32_e64 s[6:7], v168, v2
	v_cmp_lt_i32_e64 s[8:9], v168, v2
	v_cmp_gt_i32_e64 s[10:11], v135, v2
	v_cmp_gt_i32_e64 s[12:13], v169, v2
	v_cmp_gt_i32_e64 s[14:15], v170, v2
	v_cmp_gt_i32_e64 s[16:17], v171, v2
	v_cmp_gt_i32_e64 s[18:19], v172, v2
	v_cmp_gt_i32_e64 s[20:21], v173, v2
	v_cmp_gt_i32_e64 s[22:23], v174, v2
	v_cmp_gt_i32_e64 s[24:25], v175, v2
	v_cmp_gt_i32_e64 s[26:27], v176, v2
	v_cmp_gt_i32_e64 s[28:29], v177, v2
	v_cmp_gt_i32_e64 s[30:31], v178, v2
	v_cmp_gt_i32_e64 s[34:35], v179, v2
	v_cmp_gt_i32_e64 s[36:37], v180, v2
	v_cmp_gt_i32_e64 s[38:39], v181, v2
	v_cmp_gt_i32_e64 s[70:71], v6, v2
	s_min_u32 s2, s92, 8
	v_lshlrev_b32_e32 v2, 4, v4
	s_add_i32 s2, s92, s2
	v_and_b32_e32 v2, 0xc0, v2
	s_lshl_b32 s87, s2, 13
	v_lshl_or_b32 v2, v160, 8, v2
	v_readlane_b32 s2, v247, 4
	v_lshlrev_b32_e32 v5, 1, v4
	v_mov_b32_e32 v140, 0
	v_add_u32_e32 v185, s2, v2
	v_readlane_b32 s2, v247, 5
	s_movk_i32 s96, 0xc00
	s_add_i32 s91, s91, s92
	v_add_u32_e32 v187, s2, v2
	v_readlane_b32 s2, v247, 6
	s_add_i32 s93, s93, s3
	v_mov_b32_e32 v139, v131
	v_add_u32_e32 v188, s2, v2
	v_readlane_b32 s2, v247, 7
	s_mov_b32 s94, 2
	v_add_u32_e32 v183, s75, v134
	v_add_u32_e32 v189, s2, v2
	v_readlane_b32 s2, v247, 8
	v_add3_u32 v184, s76, v166, v134
	s_lshl_b32 s95, s92, 13
	v_add_u32_e32 v190, s2, v2
	v_readlane_b32 s2, v247, 9
	s_addk_i32 s87, 0x4000
	v_and_or_b32 v186, v5, 32, v3
	v_add_u32_e32 v191, s2, v2
	v_readlane_b32 s2, v247, 10
	s_add_i32 s86, s75, 0xc000
	s_mov_b32 s3, 0
	v_add_u32_e32 v192, s2, v2
	v_readlane_b32 s2, v247, 11
	v_mov_b32_e32 v202, 0
	v_mov_b32_e32 v3, v140
	v_add_u32_e32 v193, s2, v2
	v_readlane_b32 s2, v247, 12
	v_mov_b32_e32 v4, v140
	v_mov_b32_e32 v5, v140
	v_add_u32_e32 v194, s2, v2
	v_readlane_b32 s2, v247, 13
	v_mov_b32_e32 v6, v140
	v_mov_b32_e32 v7, v140
	v_add_u32_e32 v195, s2, v2
	v_readlane_b32 s2, v247, 14
	v_mov_b32_e32 v8, v140
	v_mov_b32_e32 v9, v140
	v_add_u32_e32 v196, s2, v2
	v_readlane_b32 s2, v247, 15
	v_mov_b32_e32 v10, v140
	v_mov_b32_e32 v11, v140
	v_add_u32_e32 v197, s2, v2
	v_readlane_b32 s2, v247, 16
	v_mov_b32_e32 v12, v140
	v_mov_b32_e32 v13, v140
	v_add_u32_e32 v198, s2, v2
	v_readlane_b32 s2, v247, 17
	v_mov_b32_e32 v14, v140
	v_mov_b32_e32 v15, v140
	v_add_u32_e32 v199, s2, v2
	v_readlane_b32 s2, v247, 21
	v_mov_b32_e32 v16, v140
	v_mov_b32_e32 v17, v140
	v_add_u32_e32 v200, s2, v2
	s_add_i32 s2, 0, 0x8000
	v_add_u32_e32 v201, s2, v2
	s_mov_b32 s2, 0
	v_mov_b32_e32 v2, 0
	v_mov_b32_e32 v18, 0
	v_mov_b32_e32 v19, v140
	v_mov_b32_e32 v20, v140
	v_mov_b32_e32 v21, v140
	v_mov_b32_e32 v22, v140
	v_mov_b32_e32 v23, v140
	v_add_u32_e32 v226, v201, v186
	s_nop 0
	s_nop 0
	s_nop 0
	s_nop 0
	s_nop 0
	s_nop 0
	s_nop 0
	s_nop 0
	s_nop 0
	s_nop 0
	s_nop 0
	s_nop 0
	s_nop 0
	s_nop 0
	s_nop 0
	v_mov_b32_e32 v24, v140
	v_mov_b32_e32 v25, v140
	v_mov_b32_e32 v26, v140
	v_mov_b32_e32 v27, v140
	v_mov_b32_e32 v28, v140
	v_mov_b32_e32 v29, v140
	v_mov_b32_e32 v30, v140
	v_mov_b32_e32 v31, v140
	v_mov_b32_e32 v32, v140
	v_mov_b32_e32 v33, v140
	s_mov_b32 s32, 0
	v_readlane_b32 s72, v249, 50
	s_cmp_gt_i32 s72, 7
	s_cbranch_scc1 .LBB0_2422
	s_mul_i32 s72, s72, 48
	v_readlane_b32 s73, v248, 47
	s_add_i32 s72, s73, s72
	v_readlane_b32 s78, v248, 48
	s_add_i32 s73, s72, 48
	s_min_i32 s78, s78, s73
	s_min_i32 s78, s78, 0x1be90
	v_readlane_b32 s84, v249, 16
	s_add_i32 s73, s72, s84
	s_cmp_ge_i32 s73, s78
	s_cbranch_scc1 .LBB0_2422
	v_writelane_b32 v244, s78, 3
	s_lshl_b32 s84, s84, 11
	s_add_i32 s84, s84, 0x24000
	v_and_b32_e32 v50, 63, v0
	v_and_b32_e32 v51, 31, v50
	v_lshrrev_b32_e32 v52, 5, v50
	v_lshlrev_b32_e32 v52, 10, v52
	v_lshl_add_u32 v51, v51, 2, v52
	v_add_u32_e32 v245, s84, v51
	s_mov_b32 s85, 2
	s_mov_b32 s32, 0x30
	s_branch .Lbgn_dec

.LBB0_3243:
	v_readlane_b32 s0, v249, 18
	v_readlane_b32 s1, v249, 19
	s_cmp_gt_i32 s1, 7
	v_readlane_b32 s2, v248, 17
	s_cselect_b64 s[0:1], -1, 0
	v_readlane_b32 s3, v248, 18
	s_and_b64 s[2:3], s[2:3], s[0:1]
	s_andn2_b64 vcc, exec, s[2:3]
	s_cbranch_vccnz .LBB0_3297
	s_waitcnt vmcnt(0)
	s_waitcnt vmcnt(0)
	s_barrier
	s_mov_b64 s[4:5], exec
	v_readlane_b32 s2, v249, 12
	v_readlane_b32 s3, v249, 13
	s_and_b64 s[2:3], s[4:5], s[2:3]
	s_mov_b64 exec, s[2:3]
	s_cbranch_execz .LBB0_3296
	s_nop 0
	s_nop 0
	s_nop 0
	s_nop 0
	s_nop 0
	s_nop 0
	s_nop 0
	s_nop 0
	s_nop 0
	s_nop 0
	s_nop 0
	s_nop 0
	s_nop 0
	s_nop 0
	s_nop 0
	s_nop 0
	s_nop 0
	s_nop 0
	s_nop 0
	s_nop 0
	s_nop 0
	s_nop 0
	s_nop 0
	s_nop 0
	s_nop 0
	s_nop 0
	s_nop 0
	s_nop 0
	s_nop 0
	s_nop 0
	s_nop 0
	s_nop 0
	s_nop 0
	s_nop 0
	s_nop 0
	s_nop 0
	s_nop 0
	s_nop 0
	s_nop 0
	s_nop 0
	s_nop 0
	s_nop 0
	s_nop 0
	s_nop 0
	s_nop 0
	s_nop 0
	s_nop 0
	s_nop 0
	s_add_i32 s2, 0, 0x20160
	v_mov_b32_e32 v1, s2
	s_waitcnt vmcnt(0) expcnt(0) lgkmcnt(0)
	ds_read_b32 v3, v1
	s_add_i32 s2, 0, 0x20164
	v_mov_b32_e32 v1, s2
	ds_read_b32 v1, v1
	s_waitcnt lgkmcnt(1)
	v_cmp_ne_u32_e32 vcc, 0, v3
	s_cbranch_vccnz .LBB0_3260
	v_readlane_b32 s6, v249, 3
	v_readlane_b32 s7, v249, 4
	s_load_dwordx2 s[2:3], s[6:7], 0x4
	v_readlane_b32 s6, v249, 1
	v_readlane_b32 s7, v249, 2
	s_load_dwordx4 s[40:43], s[6:7], 0xd8
	v_mov_b32_e32 v17, 0
	s_waitcnt lgkmcnt(0)
	s_mul_i32 s2, s2, s81
	s_mul_i32 s2, s2, s3
	s_mov_b32 s3, 1
	s_add_u32 s6, s42, 0x4200
	s_addc_u32 s7, s43, 0
	s_add_u32 s8, s42, 0x4400
	s_addc_u32 s9, s43, 0
	s_add_u32 s10, s42, 0x4500
	s_addc_u32 s11, s43, 0
	s_add_u32 s12, s42, 0x4600
	s_addc_u32 s13, s43, 0
	s_add_u32 s14, s42, 0x4700
	s_addc_u32 s15, s43, 0
	s_add_u32 s16, s42, 0x4800
	s_addc_u32 s17, s43, 0
	s_add_u32 s18, s42, 0x4900
	s_addc_u32 s19, s43, 0
	s_add_u32 s20, s42, 0x4a00
	s_addc_u32 s21, s43, 0
	s_add_u32 s22, s42, 0x4b00
	s_addc_u32 s23, s43, 0
	s_add_u32 s24, s42, 0x4c00
	s_addc_u32 s25, s43, 0
	s_add_u32 s26, s42, 0x4d00
	s_addc_u32 s27, s43, 0
	s_add_u32 s28, s42, 0x4e00
	s_addc_u32 s29, s43, 0
	s_add_u32 s30, s42, 0x4f00
	s_addc_u32 s31, s43, 0
	s_add_u32 s34, s42, 0x5000
	s_addc_u32 s35, s43, 0
	s_add_u32 s36, s42, 0x5100
	s_addc_u32 s37, s43, 0
	s_add_u32 s38, s42, 0x5200
	s_addc_u32 s39, s43, 0
	s_add_u32 s40, s42, 0x5300
	s_addc_u32 s41, s43, 0
	s_branch .LBB0_3248
